# baseline (speedup 1.0000x reference)
.LBB1_1:
	s_waitcnt lgkmcnt(0)
	v_mfma_f32_32x32x16_f16 v[114:129], v[198:201], v[186:189], v[114:129]
	s_mov_b32 s44, s33
	s_mov_b32 s33, s43
	v_mfma_f32_32x32x16_f16 v[98:113], v[198:201], v[182:185], v[98:113]
	v_add_u32_e32 v219, s33, v215
	ds_read_b128 v[198:201], v219 offset:8192
	ds_read_b128 v[220:223], v219 offset:10240
	ds_read_b128 v[224:227], v219 offset:12288
	ds_read_b128 v[228:231], v219 offset:14336
	v_add_u32_e32 v219, s33, v214
	ds_read_b128 v[232:235], v219
	ds_read_b128 v[236:239], v219 offset:2048
	s_waitcnt vmcnt(10)
	v_cvt_pk_f16_f32 v162, v162, v163
	v_cvt_pk_f16_f32 v163, v164, v165
	v_cvt_pk_f16_f32 v164, v154, v155
	v_cvt_pk_f16_f32 v165, v156, v157
	v_add_u32_e32 v154, s34, v209
	ds_write_b64 v154, v[162:163]
	v_add_u32_e32 v154, s34, v248
	ds_write_b64 v154, v[164:165]
	v_mfma_f32_32x32x16_f16 v[82:97], v[194:197], v[186:189], v[82:97]
	v_add_u32_e32 v154, s34, v208
	s_waitcnt vmcnt(9)
	ds_write_b128 v154, v[158:161] offset:8192
	s_waitcnt vmcnt(8)
	ds_write_b128 v154, v[174:177] offset:16384
	v_mfma_f32_32x32x16_f16 v[66:81], v[194:197], v[182:185], v[66:81]
	v_mfma_f32_32x32x16_f16 v[50:65], v[190:193], v[186:189], v[50:65]
	s_waitcnt vmcnt(7)
	ds_write_b128 v154, v[166:169] offset:24576
	s_waitcnt vmcnt(6)
	ds_write_b128 v154, v[170:173] offset:32768
	v_mfma_f32_32x32x16_f16 v[34:49], v[190:193], v[182:185], v[34:49]
	s_cmp_ge_u32 s29, 4
	s_cbranch_scc1 .Lpj_A_late
	v_add_co_u32_e64 v158, s[0:1], s36, v202
	global_load_dwordx4 v[154:157], v[252:253], off offset:-144 sc1 nt
	global_load_dwordx4 v[162:165], v[204:205], off offset:-144 sc1 nt
	v_addc_co_u32_e64 v159, s[0:1], -1, v203, s[0:1]
	v_add_co_u32_e64 v166, s[0:1], s37, v202
	v_mfma_f32_32x32x16_f16 v[18:33], v[178:181], v[186:189], v[18:33]
	s_nop 0
	v_addc_co_u32_e64 v167, s[0:1], -1, v203, s[0:1]
	global_load_dwordx4 v[158:161], v[158:159], off sc1
	s_nop 0
	global_load_dwordx4 v[174:177], v[166:167], off sc1
	v_add_co_u32_e64 v166, s[0:1], s38, v202
	s_nop 1
	v_addc_co_u32_e64 v167, s[0:1], -1, v203, s[0:1]
	v_add_co_u32_e64 v170, s[0:1], s39, v202
	v_mfma_f32_32x32x16_f16 v[2:17], v[178:181], v[182:185], v[2:17]
	s_nop 0
	v_addc_co_u32_e64 v171, s[0:1], -1, v203, s[0:1]
	global_load_dwordx4 v[166:169], v[166:167], off sc1
	s_nop 0
	global_load_dwordx4 v[170:173], v[170:171], off sc1
.Lpj_A_join:
	v_add_u32_e32 v190, s44, v216
	ds_read_b128 v[178:181], v190 offset:8192
	ds_read_b128 v[182:185], v190 offset:10240
	ds_read_b128 v[186:189], v190 offset:12288
	ds_read_b128 v[190:193], v190 offset:14336
	v_add_u32_e32 v219, s44, v217
	ds_read_b128 v[194:197], v219
	ds_read_b128 v[240:243], v219 offset:2048
	s_waitcnt lgkmcnt(12)
	v_mfma_f32_32x32x16_f16 v[114:129], v[198:201], v[232:235], v[114:129]
	s_waitcnt lgkmcnt(11)
	v_mfma_f32_32x32x16_f16 v[98:113], v[198:201], v[236:239], v[98:113]
	v_mfma_f32_32x32x16_f16 v[82:97], v[220:223], v[232:235], v[82:97]
	s_cmp_lt_u32 s29, 4
	s_cbranch_scc1 .Lpj_A_s1
	v_add_co_u32_e64 v158, s[0:1], s36, v202
	global_load_dwordx4 v[154:157], v[252:253], off offset:-144 sc1 nt
	global_load_dwordx4 v[162:165], v[204:205], off offset:-144 sc1 nt
	v_addc_co_u32_e64 v159, s[0:1], -1, v203, s[0:1]
	v_add_co_u32_e64 v166, s[0:1], s37, v202
	s_nop 1
	v_addc_co_u32_e64 v167, s[0:1], -1, v203, s[0:1]
	global_load_dwordx4 v[158:161], v[158:159], off sc1
	s_nop 0
	global_load_dwordx4 v[174:177], v[166:167], off sc1
.Lpj_A_s1:
	v_mfma_f32_32x32x16_f16 v[66:81], v[220:223], v[236:239], v[66:81]
	v_mfma_f32_32x32x16_f16 v[50:65], v[224:227], v[232:235], v[50:65]
	v_mfma_f32_32x32x16_f16 v[34:49], v[224:227], v[236:239], v[34:49]
	s_cmp_lt_u32 s29, 4
	s_cbranch_scc1 .Lpj_A_s2
	v_add_co_u32_e64 v166, s[0:1], s38, v202
	s_nop 1
	v_addc_co_u32_e64 v167, s[0:1], -1, v203, s[0:1]
	v_add_co_u32_e64 v170, s[0:1], s39, v202
	s_nop 1
	v_addc_co_u32_e64 v171, s[0:1], -1, v203, s[0:1]
	global_load_dwordx4 v[166:169], v[166:167], off sc1
	s_nop 0
	global_load_dwordx4 v[170:173], v[170:171], off sc1
.Lpj_A_s2:
	v_mfma_f32_32x32x16_f16 v[18:33], v[228:231], v[232:235], v[18:33]
	v_mfma_f32_32x32x16_f16 v[2:17], v[228:231], v[236:239], v[2:17]
	s_waitcnt lgkmcnt(1)
	v_mfma_f32_32x32x16_f16 v[114:129], v[178:181], v[194:197], v[114:129]
	s_waitcnt lgkmcnt(0)
	s_barrier
	s_waitcnt lgkmcnt(0)
	v_mfma_f32_32x32x16_f16 v[98:113], v[178:181], v[240:243], v[98:113]
	v_add_u32_e32 v178, s44, v215
	ds_read_b128 v[220:223], v178 offset:8192
	ds_read_b128 v[224:227], v178 offset:10240
	ds_read_b128 v[228:231], v178 offset:12288
	ds_read_b128 v[232:235], v178 offset:14336
	v_add_u32_e32 v178, s44, v214
	ds_read_b128 v[236:239], v178
	ds_read_b128 v[244:247], v178 offset:2048
	s_waitcnt vmcnt(10)
	v_cvt_pk_f16_f32 v150, v150, v151
	v_cvt_pk_f16_f32 v151, v152, v153
	v_cvt_pk_f16_f32 v152, v142, v143
	v_cvt_pk_f16_f32 v153, v144, v145
	v_add_u32_e32 v142, s33, v209
	ds_write_b64 v142, v[150:151]
	v_add_u32_e32 v142, s33, v248
	ds_write_b64 v142, v[152:153]
	v_mfma_f32_32x32x16_f16 v[82:97], v[182:185], v[194:197], v[82:97]
	v_add_u32_e32 v142, s33, v208
	s_waitcnt vmcnt(9)
	ds_write_b128 v142, v[138:141] offset:8192
	s_waitcnt vmcnt(8)
	ds_write_b128 v142, v[146:149] offset:16384
	v_mfma_f32_32x32x16_f16 v[66:81], v[182:185], v[240:243], v[66:81]
	v_mfma_f32_32x32x16_f16 v[50:65], v[186:189], v[194:197], v[50:65]
	s_waitcnt vmcnt(7)
	ds_write_b128 v142, v[134:137] offset:24576
	s_waitcnt vmcnt(6)
	ds_write_b128 v142, v[130:133] offset:32768
	v_mfma_f32_32x32x16_f16 v[34:49], v[186:189], v[240:243], v[34:49]
	s_cmp_ge_u32 s29, 4
	s_cbranch_scc1 .Lpj_B_late
	v_add_co_u32_e64 v130, s[0:1], s40, v202
	global_load_dwordx4 v[142:145], v[252:253], off offset:-16 sc1 nt
	global_load_dwordx4 v[150:153], v[204:205], off offset:-16 sc1 nt
	v_addc_co_u32_e64 v131, s[0:1], -1, v203, s[0:1]
	v_add_co_u32_e64 v132, s[0:1], s41, v202
	v_mfma_f32_32x32x16_f16 v[18:33], v[190:193], v[194:197], v[18:33]
	s_nop 0
	v_addc_co_u32_e64 v133, s[0:1], -1, v203, s[0:1]
	global_load_dwordx4 v[138:141], v[130:131], off sc1
	global_load_dwordx4 v[146:149], v[132:133], off sc1
	v_add_co_u32_e64 v130, s[0:1], s42, v202
	s_nop 1
	v_addc_co_u32_e64 v131, s[0:1], -1, v203, s[0:1]
	global_load_dwordx4 v[134:137], v[130:131], off sc1
	s_nop 0
	global_load_dwordx4 v[130:133], v[202:203], off sc1
	v_mfma_f32_32x32x16_f16 v[2:17], v[190:193], v[240:243], v[2:17]
.Lpj_B_join:
	v_add_u32_e32 v178, s34, v216
	ds_read_b128 v[198:201], v178 offset:8192
	ds_read_b128 v[194:197], v178 offset:10240
	ds_read_b128 v[190:193], v178 offset:12288
	ds_read_b128 v[178:181], v178 offset:14336
	v_add_u32_e32 v182, s34, v217
	ds_read_b128 v[186:189], v182
	ds_read_b128 v[182:185], v182 offset:2048
	s_waitcnt lgkmcnt(12)
	v_mfma_f32_32x32x16_f16 v[114:129], v[220:223], v[236:239], v[114:129]
	s_waitcnt lgkmcnt(11)
	v_mfma_f32_32x32x16_f16 v[98:113], v[220:223], v[244:247], v[98:113]
	v_mfma_f32_32x32x16_f16 v[82:97], v[224:227], v[236:239], v[82:97]
	s_cmp_lt_u32 s29, 4
	s_cbranch_scc1 .Lpj_B_s1
	v_add_co_u32_e64 v130, s[0:1], s40, v202
	global_load_dwordx4 v[142:145], v[252:253], off offset:-16 sc1 nt
	global_load_dwordx4 v[150:153], v[204:205], off offset:-16 sc1 nt
	v_addc_co_u32_e64 v131, s[0:1], -1, v203, s[0:1]
	v_add_co_u32_e64 v132, s[0:1], s41, v202
	s_nop 1
	v_addc_co_u32_e64 v133, s[0:1], -1, v203, s[0:1]
	global_load_dwordx4 v[138:141], v[130:131], off sc1
	global_load_dwordx4 v[146:149], v[132:133], off sc1
.Lpj_B_s1:
	v_mfma_f32_32x32x16_f16 v[66:81], v[224:227], v[244:247], v[66:81]
	v_mfma_f32_32x32x16_f16 v[50:65], v[228:231], v[236:239], v[50:65]
	v_mfma_f32_32x32x16_f16 v[34:49], v[228:231], v[244:247], v[34:49]
	s_cmp_lt_u32 s29, 4
	s_cbranch_scc1 .Lpj_B_s2
	v_add_co_u32_e64 v130, s[0:1], s42, v202
	s_nop 1
	v_addc_co_u32_e64 v131, s[0:1], -1, v203, s[0:1]
	global_load_dwordx4 v[134:137], v[130:131], off sc1
	s_nop 0
	global_load_dwordx4 v[130:133], v[202:203], off sc1
.Lpj_B_s2:
	v_mfma_f32_32x32x16_f16 v[18:33], v[232:235], v[236:239], v[18:33]
	v_mfma_f32_32x32x16_f16 v[2:17], v[232:235], v[244:247], v[2:17]
	s_waitcnt lgkmcnt(0)
	s_barrier
	s_add_i32 s35, s35, 2
	v_lshl_add_u64 v[202:203], v[202:203], 0, s[24:25]
	v_lshl_add_u64 v[204:205], v[204:205], 0, s[26:27]
	v_lshl_add_u64 v[252:253], v[252:253], 0, s[26:27]
	s_mov_b32 s43, s34
	s_cmp_gt_u32 s35, 9
	s_mov_b32 s34, s44
	s_cbranch_scc0 .LBB1_1
	s_and_b64 s[0:1], s[20:21], exec
	s_cselect_b32 s6, s6, s8
	s_cselect_b32 s7, s7, s9
	s_and_b64 s[0:1], vcc, exec
	s_cselect_b32 s1, s5, s7
	s_cselect_b32 s0, s4, s6
	v_mov_b32_e32 v202, 0x3e38aa3b
	s_waitcnt lgkmcnt(1)
	v_mfma_f32_32x32x16_f16 v[114:129], v[198:201], v[186:189], v[114:129]
	v_cndmask_b32_e32 v202, 1.0, v202, vcc
	s_waitcnt lgkmcnt(0)
	v_mfma_f32_32x32x16_f16 v[98:113], v[198:201], v[182:185], v[98:113]
	ds_read_b128 v[198:201], v215 offset:8192
	ds_read_b128 v[220:223], v215 offset:10240
	ds_read_b128 v[224:227], v215 offset:12288
	ds_read_b128 v[228:231], v215 offset:14336
	ds_read_b128 v[232:235], v214
	ds_read_b128 v[236:239], v214 offset:2048
	s_waitcnt vmcnt(10)
	v_cvt_pk_f16_f32 v162, v162, v163
	v_cvt_pk_f16_f32 v163, v164, v165
	v_cvt_pk_f16_f32 v164, v154, v155
	v_cvt_pk_f16_f32 v165, v156, v157
	v_add_u32_e32 v154, 0x14000, v209
	ds_write_b64 v154, v[162:163]
	v_add_u32_e32 v154, 0x14000, v248
	ds_write_b64 v154, v[164:165]
	v_add_u32_e32 v154, 0x14000, v213
	s_waitcnt vmcnt(9)
	ds_write_b128 v154, v[158:161]
	v_add_u32_e32 v154, 0x16000, v213
	v_mfma_f32_32x32x16_f16 v[82:97], v[194:197], v[186:189], v[82:97]
	s_waitcnt vmcnt(8)
	ds_write_b128 v154, v[174:177]
	v_mfma_f32_32x32x16_f16 v[66:81], v[194:197], v[182:185], v[66:81]
	v_add_u32_e32 v154, 0x18000, v213
	s_waitcnt vmcnt(7)
	ds_write_b128 v154, v[166:169]
	v_add_u32_e32 v154, 0x1a000, v213
	v_mfma_f32_32x32x16_f16 v[50:65], v[190:193], v[186:189], v[50:65]
	s_waitcnt vmcnt(6)
	ds_write_b128 v154, v[170:173]
	v_mfma_f32_32x32x16_f16 v[34:49], v[190:193], v[182:185], v[34:49]
	v_mfma_f32_32x32x16_f16 v[18:33], v[178:181], v[186:189], v[18:33]
	v_mfma_f32_32x32x16_f16 v[2:17], v[178:181], v[182:185], v[2:17]
	ds_read_b128 v[154:157], v216 offset:49152
	ds_read_b128 v[158:161], v216 offset:51200
	ds_read_b128 v[162:165], v216 offset:53248
	ds_read_b128 v[166:169], v216 offset:55296
	ds_read_b128 v[170:173], v217 offset:40960
	ds_read_b128 v[174:177], v217 offset:43008
	s_waitcnt lgkmcnt(12)
	v_mfma_f32_32x32x16_f16 v[114:129], v[198:201], v[232:235], v[114:129]
	s_waitcnt lgkmcnt(11)
	v_mfma_f32_32x32x16_f16 v[98:113], v[198:201], v[236:239], v[98:113]
	v_mfma_f32_32x32x16_f16 v[82:97], v[220:223], v[232:235], v[82:97]
	v_mfma_f32_32x32x16_f16 v[66:81], v[220:223], v[236:239], v[66:81]
	v_mfma_f32_32x32x16_f16 v[50:65], v[224:227], v[232:235], v[50:65]
	v_mfma_f32_32x32x16_f16 v[34:49], v[224:227], v[236:239], v[34:49]
	v_mfma_f32_32x32x16_f16 v[18:33], v[228:231], v[232:235], v[18:33]
	v_mfma_f32_32x32x16_f16 v[2:17], v[228:231], v[236:239], v[2:17]
	s_waitcnt lgkmcnt(0)
	s_barrier
	s_waitcnt lgkmcnt(1)
	v_mfma_f32_32x32x16_f16 v[114:129], v[154:157], v[170:173], v[114:129]
	s_waitcnt lgkmcnt(0)
	v_mfma_f32_32x32x16_f16 v[98:113], v[154:157], v[174:177], v[98:113]
	ds_read_b128 v[154:157], v215 offset:49152
	ds_read_b128 v[178:181], v215 offset:51200
	ds_read_b128 v[182:185], v215 offset:53248
	ds_read_b128 v[186:189], v215 offset:55296
	ds_read_b128 v[190:193], v214 offset:40960
	ds_read_b128 v[194:197], v214 offset:43008
	s_waitcnt vmcnt(4)
	v_cvt_pk_f16_f32 v150, v150, v151
	v_cvt_pk_f16_f32 v151, v152, v153
	v_cvt_pk_f16_f32 v152, v142, v143
	v_cvt_pk_f16_f32 v153, v144, v145
	ds_write_b64 v209, v[150:151]
	ds_write_b64 v248, v[152:153]
	v_mfma_f32_32x32x16_f16 v[82:97], v[158:161], v[170:173], v[82:97]
	s_waitcnt vmcnt(3)
	ds_write_b128 v208, v[138:141] offset:8192
	s_waitcnt vmcnt(2)
	ds_write_b128 v208, v[146:149] offset:16384
	v_mfma_f32_32x32x16_f16 v[66:81], v[158:161], v[174:177], v[66:81]
	v_mfma_f32_32x32x16_f16 v[50:65], v[162:165], v[170:173], v[50:65]
	s_waitcnt vmcnt(1)
	ds_write_b128 v208, v[134:137] offset:24576
	s_waitcnt vmcnt(0)
	ds_write_b128 v208, v[130:133] offset:32768
	v_mfma_f32_32x32x16_f16 v[34:49], v[162:165], v[174:177], v[34:49]
	v_mfma_f32_32x32x16_f16 v[18:33], v[166:169], v[170:173], v[18:33]
	v_mfma_f32_32x32x16_f16 v[2:17], v[166:169], v[174:177], v[2:17]
	v_add_u32_e32 v158, 0x16000, v211
	v_add_u32_e32 v142, v158, v210
	ds_read_b128 v[130:133], v142
	ds_read_b128 v[134:137], v142 offset:2048
	ds_read_b128 v[138:141], v142 offset:4096
	ds_read_b128 v[142:145], v142 offset:6144
	v_add_u32_e32 v166, 0x14000, v218
	v_add_u32_e32 v150, v166, v210
	ds_read_b128 v[146:149], v150
	ds_read_b128 v[150:153], v150 offset:2048
	s_waitcnt lgkmcnt(12)
	v_mfma_f32_32x32x16_f16 v[114:129], v[154:157], v[190:193], v[114:129]
	s_waitcnt lgkmcnt(11)
	v_mfma_f32_32x32x16_f16 v[98:113], v[154:157], v[194:197], v[98:113]
	v_mfma_f32_32x32x16_f16 v[82:97], v[178:181], v[190:193], v[82:97]
	v_mfma_f32_32x32x16_f16 v[66:81], v[178:181], v[194:197], v[66:81]
	v_mfma_f32_32x32x16_f16 v[50:65], v[182:185], v[190:193], v[50:65]
	v_mfma_f32_32x32x16_f16 v[34:49], v[182:185], v[194:197], v[34:49]
	v_mfma_f32_32x32x16_f16 v[18:33], v[186:189], v[190:193], v[18:33]
	v_mfma_f32_32x32x16_f16 v[2:17], v[186:189], v[194:197], v[2:17]
	s_waitcnt lgkmcnt(0)
	s_barrier
	s_waitcnt lgkmcnt(1)
	v_mfma_f32_32x32x16_f16 v[114:129], v[130:133], v[146:149], v[114:129]
	s_waitcnt lgkmcnt(0)
	v_mfma_f32_32x32x16_f16 v[98:113], v[130:133], v[150:153], v[98:113]
	v_add_u32_e32 v162, v158, v212
	ds_read_b128 v[130:133], v162
	ds_read_b128 v[154:157], v162 offset:2048
	ds_read_b128 v[158:161], v162 offset:4096
	ds_read_b128 v[162:165], v162 offset:6144
	v_add_u32_e32 v170, v166, v212
	ds_read_b128 v[166:169], v170
	ds_read_b128 v[170:173], v170 offset:2048
	v_mfma_f32_32x32x16_f16 v[82:97], v[134:137], v[146:149], v[82:97]
	v_mfma_f32_32x32x16_f16 v[66:81], v[134:137], v[150:153], v[66:81]
	v_mfma_f32_32x32x16_f16 v[50:65], v[138:141], v[146:149], v[50:65]
	v_mfma_f32_32x32x16_f16 v[34:49], v[138:141], v[150:153], v[34:49]
	v_mfma_f32_32x32x16_f16 v[18:33], v[142:145], v[146:149], v[18:33]
	v_mfma_f32_32x32x16_f16 v[2:17], v[142:145], v[150:153], v[2:17]
	ds_read_b128 v[134:137], v216 offset:8192
	ds_read_b128 v[138:141], v216 offset:10240
	ds_read_b128 v[142:145], v216 offset:12288
	ds_read_b128 v[146:149], v216 offset:14336
	ds_read_b128 v[150:153], v217
	ds_read_b128 v[174:177], v217 offset:2048
	s_waitcnt lgkmcnt(7)
	v_mfma_f32_32x32x16_f16 v[114:129], v[130:133], v[166:169], v[114:129]
	s_waitcnt lgkmcnt(6)
	v_mfma_f32_32x32x16_f16 v[98:113], v[130:133], v[170:173], v[98:113]
	v_mfma_f32_32x32x16_f16 v[82:97], v[154:157], v[166:169], v[82:97]
	v_mfma_f32_32x32x16_f16 v[66:81], v[154:157], v[170:173], v[66:81]
	v_mfma_f32_32x32x16_f16 v[50:65], v[158:161], v[166:169], v[50:65]
	v_mfma_f32_32x32x16_f16 v[34:49], v[158:161], v[170:173], v[34:49]
	v_mfma_f32_32x32x16_f16 v[18:33], v[162:165], v[166:169], v[18:33]
	v_mfma_f32_32x32x16_f16 v[2:17], v[162:165], v[170:173], v[2:17]
	s_waitcnt lgkmcnt(0)
	s_barrier
	s_waitcnt lgkmcnt(1)
	v_mfma_f32_32x32x16_f16 v[114:129], v[134:137], v[150:153], v[114:129]
	s_waitcnt lgkmcnt(0)
	v_mfma_f32_32x32x16_f16 v[98:113], v[134:137], v[174:177], v[98:113]
	ds_read_b128 v[130:133], v215 offset:8192
	ds_read_b128 v[134:137], v215 offset:10240
	ds_read_b128 v[154:157], v215 offset:12288
	ds_read_b128 v[158:161], v215 offset:14336
	ds_read_b128 v[162:165], v214
	ds_read_b128 v[166:169], v214 offset:2048
	v_mfma_f32_32x32x16_f16 v[82:97], v[138:141], v[150:153], v[82:97]
	v_mfma_f32_32x32x16_f16 v[66:81], v[138:141], v[174:177], v[66:81]
	v_mfma_f32_32x32x16_f16 v[50:65], v[142:145], v[150:153], v[50:65]
	v_mfma_f32_32x32x16_f16 v[34:49], v[142:145], v[174:177], v[34:49]
	v_mfma_f32_32x32x16_f16 v[18:33], v[146:149], v[150:153], v[18:33]
	v_mfma_f32_32x32x16_f16 v[2:17], v[146:149], v[174:177], v[2:17]
	s_waitcnt lgkmcnt(1)
	v_mfma_f32_32x32x16_f16 v[114:129], v[130:133], v[162:165], v[114:129]
	s_waitcnt lgkmcnt(0)
	v_mfma_f32_32x32x16_f16 v[98:113], v[130:133], v[166:169], v[98:113]
	v_mfma_f32_32x32x16_f16 v[82:97], v[134:137], v[162:165], v[82:97]
	v_mfma_f32_32x32x16_f16 v[66:81], v[134:137], v[166:169], v[66:81]
	v_mfma_f32_32x32x16_f16 v[50:65], v[154:157], v[162:165], v[50:65]
	v_mfma_f32_32x32x16_f16 v[34:49], v[154:157], v[166:169], v[34:49]
	v_mfma_f32_32x32x16_f16 v[18:33], v[158:161], v[162:165], v[18:33]
	v_mfma_f32_32x32x16_f16 v[2:17], v[158:161], v[166:169], v[2:17]
	v_lshl_or_b32 v130, v207, 2, s31
	s_waitcnt lgkmcnt(0)
	s_barrier
	s_cbranch_vccnz .Lepi_q
	v_lshlrev_b32_e32 v154, 2, v130
	global_load_dwordx4 v[134:137], v154, s[0:1]
	global_load_dwordx4 v[150:153], v154, s[0:1] offset:32
	global_load_dwordx4 v[156:159], v154, s[0:1] offset:64
	global_load_dwordx4 v[160:163], v154, s[0:1] offset:96
	global_load_dwordx4 v[164:167], v154, s[0:1] offset:128
	global_load_dwordx4 v[168:171], v154, s[0:1] offset:160
	s_movk_i32 s4, 0x410
	v_lshlrev_b32_e32 v130, 1, v130
	v_mul_lo_u32 v131, v206, s4
	v_add3_u32 v155, 0, v130, v131
	global_load_dwordx4 v[172:175], v154, s[0:1] offset:192
	global_load_dwordx4 v[146:149], v154, s[0:1] offset:224
	global_load_dwordx4 v[142:145], v154, s[0:1] offset:256
	global_load_dwordx4 v[130:133], v154, s[0:1] offset:288
	global_load_dwordx4 v[138:141], v154, s[0:1] offset:320
	v_add_u32_e32 v176, 0x8000, v155
	s_waitcnt vmcnt(10)
	v_pk_add_f32 v[114:115], v[134:135], v[114:115]
	v_pk_add_f32 v[116:117], v[136:137], v[116:117]
	v_pk_add_f32 v[98:99], v[134:135], v[98:99]
	v_pk_add_f32 v[100:101], v[136:137], v[100:101]
	s_waitcnt vmcnt(9)
	v_pk_add_f32 v[118:119], v[150:151], v[118:119]
	v_pk_add_f32 v[120:121], v[152:153], v[120:121]
	s_waitcnt vmcnt(6)
	v_pk_add_f32 v[82:83], v[164:165], v[82:83]
	v_pk_add_f32 v[84:85], v[166:167], v[84:85]
	v_pk_add_f32 v[66:67], v[164:165], v[66:67]
	v_pk_add_f32 v[68:69], v[166:167], v[68:69]
	s_waitcnt vmcnt(5)
	v_pk_add_f32 v[70:71], v[168:169], v[70:71]
	v_pk_add_f32 v[72:73], v[170:171], v[72:73]
	v_pk_add_f32 v[102:103], v[150:151], v[102:103]
	v_pk_add_f32 v[104:105], v[152:153], v[104:105]
	v_pk_add_f32 v[122:123], v[156:157], v[122:123]
	v_pk_add_f32 v[124:125], v[158:159], v[124:125]
	v_pk_add_f32 v[106:107], v[156:157], v[106:107]
	v_pk_add_f32 v[108:109], v[158:159], v[108:109]
	v_pk_add_f32 v[126:127], v[160:161], v[126:127]
	v_pk_add_f32 v[128:129], v[162:163], v[128:129]
	v_pk_add_f32 v[110:111], v[160:161], v[110:111]
	v_pk_add_f32 v[112:113], v[162:163], v[112:113]
	v_pk_add_f32 v[86:87], v[168:169], v[86:87]
	v_pk_add_f32 v[88:89], v[170:171], v[88:89]
	v_cvt_pk_f16_f32 v114, v114, v115
	v_cvt_pk_f16_f32 v115, v116, v117
	v_cvt_pk_f16_f32 v98, v98, v99
	v_cvt_pk_f16_f32 v99, v100, v101
	v_cvt_pk_f16_f32 v100, v118, v119
	v_cvt_pk_f16_f32 v101, v120, v121
	v_cvt_pk_f16_f32 v82, v82, v83
	v_cvt_pk_f16_f32 v83, v84, v85
	v_cvt_pk_f16_f32 v84, v66, v67
	v_cvt_pk_f16_f32 v85, v68, v69
	v_cvt_pk_f16_f32 v70, v70, v71
	v_cvt_pk_f16_f32 v71, v72, v73
	v_cvt_pk_f16_f32 v102, v102, v103
	v_cvt_pk_f16_f32 v103, v104, v105
	v_cvt_pk_f16_f32 v104, v122, v123
	v_cvt_pk_f16_f32 v105, v124, v125
	v_cvt_pk_f16_f32 v106, v106, v107
	v_cvt_pk_f16_f32 v107, v108, v109
	v_cvt_pk_f16_f32 v108, v126, v127
	v_cvt_pk_f16_f32 v109, v128, v129
	v_cvt_pk_f16_f32 v110, v110, v111
	v_cvt_pk_f16_f32 v111, v112, v113
	v_cvt_pk_f16_f32 v86, v86, v87
	ds_write2_b64 v155, v[114:115], v[100:101] offset1:2
	ds_write2_b64 v176, v[98:99], v[102:103] offset0:64 offset1:66
	ds_write2_b64 v155, v[104:105], v[108:109] offset0:4 offset1:6
	ds_write2_b64 v176, v[106:107], v[110:111] offset0:68 offset1:70
	v_cvt_pk_f16_f32 v87, v88, v89
	ds_write2_b64 v176, v[84:85], v[70:71] offset0:72 offset1:74
	s_waitcnt vmcnt(4)
	v_pk_add_f32 v[70:71], v[172:173], v[90:91]
	v_pk_add_f32 v[84:85], v[174:175], v[92:93]
	v_pk_add_f32 v[74:75], v[172:173], v[74:75]
	ds_write2_b64 v155, v[82:83], v[86:87] offset0:8 offset1:10
	v_mov_b64_e32 v[82:83], v[70:71]
	global_load_dwordx4 v[66:69], v154, s[0:1] offset:352
	global_load_dwordx4 v[70:73], v154, s[0:1] offset:384
	v_cvt_pk_f16_f32 v82, v82, v83
	v_cvt_pk_f16_f32 v83, v84, v85
	v_cvt_pk_f16_f32 v84, v74, v75
	v_pk_add_f32 v[74:75], v[174:175], v[76:77]
	s_waitcnt vmcnt(5)
	v_pk_add_f32 v[78:79], v[146:147], v[78:79]
	v_cvt_pk_f16_f32 v85, v74, v75
	global_load_dwordx4 v[74:77], v154, s[0:1] offset:416
	v_pk_add_f32 v[80:81], v[148:149], v[80:81]
	v_cvt_pk_f16_f32 v78, v78, v79
	v_cvt_pk_f16_f32 v79, v80, v81
	ds_write2_b64 v176, v[84:85], v[78:79] offset0:76 offset1:78
	global_load_dwordx4 v[78:81], v154, s[0:1] offset:448
	v_pk_add_f32 v[86:87], v[146:147], v[94:95]
	v_pk_add_f32 v[88:89], v[148:149], v[96:97]
	s_waitcnt vmcnt(6)
	v_pk_add_f32 v[50:51], v[142:143], v[50:51]
	v_pk_add_f32 v[52:53], v[144:145], v[52:53]
	v_pk_add_f32 v[34:35], v[142:143], v[34:35]
	v_cvt_pk_f16_f32 v86, v86, v87
	v_cvt_pk_f16_f32 v87, v88, v89
	v_cvt_pk_f16_f32 v50, v50, v51
	v_cvt_pk_f16_f32 v51, v52, v53
	v_cvt_pk_f16_f32 v52, v34, v35
	v_pk_add_f32 v[34:35], v[144:145], v[36:37]
	ds_write2_b64 v155, v[82:83], v[86:87] offset0:12 offset1:14
	v_mov_b64_e32 v[82:83], v[34:35]
	global_load_dwordx4 v[34:37], v154, s[0:1] offset:480
	s_waitcnt vmcnt(6)
	v_pk_add_f32 v[38:39], v[130:131], v[38:39]
	v_pk_add_f32 v[40:41], v[132:133], v[40:41]
	v_cvt_pk_f16_f32 v53, v82, v83
	v_cvt_pk_f16_f32 v38, v38, v39
	v_cvt_pk_f16_f32 v39, v40, v41
	ds_write2_b64 v176, v[52:53], v[38:39] offset0:80 offset1:82
	s_waitcnt vmcnt(5)
	v_pk_add_f32 v[38:39], v[138:139], v[58:59]
	v_pk_add_f32 v[40:41], v[140:141], v[60:61]
	v_cvt_pk_f16_f32 v38, v38, v39
	v_cvt_pk_f16_f32 v39, v40, v41
	v_pk_add_f32 v[40:41], v[138:139], v[42:43]
	v_pk_add_f32 v[42:43], v[140:141], v[44:45]
	v_cvt_pk_f16_f32 v40, v40, v41
	v_cvt_pk_f16_f32 v41, v42, v43
	v_pk_add_f32 v[54:55], v[130:131], v[54:55]
	v_pk_add_f32 v[56:57], v[132:133], v[56:57]
	v_cmp_gt_u32_e64 s[0:1], 8, v0
	v_cvt_pk_f16_f32 v54, v54, v55
	v_cvt_pk_f16_f32 v55, v56, v57
	s_and_b64 s[6:7], s[20:21], s[0:1]
	ds_write2_b64 v155, v[50:51], v[54:55] offset0:16 offset1:18
	s_waitcnt vmcnt(4)
	v_pk_add_f32 v[42:43], v[66:67], v[62:63]
	s_waitcnt vmcnt(3)
	v_pk_add_f32 v[18:19], v[70:71], v[18:19]
	v_pk_add_f32 v[20:21], v[72:73], v[20:21]
	v_pk_add_f32 v[2:3], v[70:71], v[2:3]
	v_pk_add_f32 v[4:5], v[72:73], v[4:5]
	v_cvt_pk_f16_f32 v18, v18, v19
	v_cvt_pk_f16_f32 v19, v20, v21
	v_cvt_pk_f16_f32 v2, v2, v3
	v_cvt_pk_f16_f32 v3, v4, v5
	s_waitcnt vmcnt(2)
	v_pk_add_f32 v[4:5], v[74:75], v[22:23]
	v_pk_add_f32 v[20:21], v[76:77], v[24:25]
	v_cvt_pk_f16_f32 v4, v4, v5
	v_cvt_pk_f16_f32 v5, v20, v21
	ds_write2_b64 v155, v[18:19], v[4:5] offset0:24 offset1:26
	v_pk_add_f32 v[4:5], v[74:75], v[6:7]
	v_pk_add_f32 v[6:7], v[76:77], v[8:9]
	v_cvt_pk_f16_f32 v4, v4, v5
	v_cvt_pk_f16_f32 v5, v6, v7
	ds_write2_b64 v176, v[2:3], v[4:5] offset0:88 offset1:90
	s_waitcnt vmcnt(1)
	v_pk_add_f32 v[2:3], v[78:79], v[26:27]
	v_pk_add_f32 v[4:5], v[80:81], v[28:29]
	v_cvt_pk_f16_f32 v2, v2, v3
	v_cvt_pk_f16_f32 v3, v4, v5
	v_pk_add_f32 v[4:5], v[78:79], v[10:11]
	v_pk_add_f32 v[6:7], v[80:81], v[12:13]
	v_pk_add_f32 v[44:45], v[68:69], v[64:65]
	v_cvt_pk_f16_f32 v4, v4, v5
	v_cvt_pk_f16_f32 v5, v6, v7
	s_waitcnt vmcnt(0)
	v_pk_add_f32 v[6:7], v[34:35], v[30:31]
	v_pk_add_f32 v[8:9], v[36:37], v[32:33]
	v_cvt_pk_f16_f32 v42, v42, v43
	v_cvt_pk_f16_f32 v43, v44, v45
	v_cvt_pk_f16_f32 v6, v6, v7
	v_cvt_pk_f16_f32 v7, v8, v9
	ds_write2_b64 v155, v[38:39], v[42:43] offset0:20 offset1:22
	v_pk_add_f32 v[38:39], v[66:67], v[46:47]
	v_pk_add_f32 v[42:43], v[68:69], v[48:49]
	ds_write2_b64 v155, v[2:3], v[6:7] offset0:28 offset1:30
	v_pk_add_f32 v[2:3], v[34:35], v[14:15]
	v_pk_add_f32 v[6:7], v[36:37], v[16:17]
	v_cvt_pk_f16_f32 v38, v38, v39
	v_cvt_pk_f16_f32 v39, v42, v43
	v_cvt_pk_f16_f32 v2, v2, v3
	v_cvt_pk_f16_f32 v3, v6, v7
	ds_write2_b64 v176, v[40:41], v[38:39] offset0:84 offset1:86
	ds_write2_b64 v176, v[4:5], v[2:3] offset0:92 offset1:94
	s_branch .Lepi_join

.Lpj_A_late:
	v_mfma_f32_32x32x16_f16 v[18:33], v[178:181], v[186:189], v[18:33]
	v_mfma_f32_32x32x16_f16 v[2:17], v[178:181], v[182:185], v[2:17]
	s_branch .Lpj_A_join
.Lpj_B_late:
	v_mfma_f32_32x32x16_f16 v[18:33], v[190:193], v[194:197], v[18:33]
	v_mfma_f32_32x32x16_f16 v[2:17], v[190:193], v[240:243], v[2:17]
	s_branch .Lpj_B_join
